# v_T with the unit-scale v_mfma_scale f8 MFMAs of the K-loops written in the plain v_mfma_f32_16x16x128_f8f6f4 form (same e4m3 operands, 8-byte encoding, no scale-register reads)
# baseline (speedup 1.0000x reference)
.LBB0_318:
	ds_read_b128 v[26:29], v185
	ds_read_b128 v[30:33], v185 offset:1024
	ds_read_b128 v[18:21], v185 offset:2048
	ds_read_b128 v[22:25], v185 offset:3072
	ds_read_b128 v[10:13], v186
	ds_read_b128 v[14:17], v186 offset:1024
	ds_read_b128 v[2:5], v186 offset:2048
	ds_read_b128 v[6:9], v186 offset:3072
	s_add_u32 s24, s26, 0xffea8080
	s_addc_u32 s25, s27, -1
	s_cmpk_eq_i32 s58, 0x52
	s_cselect_b32 s31, s5, s25
	s_cselect_b32 s30, s4, s24
	s_cselect_b32 s29, s21, s51
	s_cselect_b32 s28, s20, s50
	v_lshl_add_u64 v[212:213], s[26:27], 0, v[166:167]
	s_add_i32 m0, s7, 0xc000
	ds_read_b128 v[174:177], v187
	ds_read_b128 v[178:181], v187 offset:1024
	ds_read_b128 v[188:191], v187 offset:2048
	ds_read_b128 v[192:195], v187 offset:3072
	ds_read_b128 v[196:199], v187 offset:4096
	ds_read_b128 v[200:203], v187 offset:5120
	ds_read_b128 v[204:207], v187 offset:6144
	ds_read_b128 v[208:211], v187 offset:7168
	global_load_lds_dwordx4 v[212:213], off
	v_lshl_add_u64 v[212:213], s[26:27], 0, v[168:169]
	s_add_i32 m0, s7, 0xe000
	s_nop 0
	global_load_lds_dwordx4 v[212:213], off
	s_waitcnt vmcnt(8)
	s_waitcnt lgkmcnt(0)
	s_barrier
	s_setprio 1
	s_waitcnt lgkmcnt(0)
	v_mfma_f32_16x16x128_f8f6f4 v[158:161], v[26:33], v[174:181], v[158:161]
	v_mfma_f32_16x16x128_f8f6f4 v[154:157], v[18:25], v[174:181], v[154:157]
	v_mfma_f32_16x16x128_f8f6f4 v[138:141], v[18:25], v[188:195], v[138:141]
	v_mfma_f32_16x16x128_f8f6f4 v[142:145], v[26:33], v[188:195], v[142:145]
	v_mfma_f32_16x16x128_f8f6f4 v[126:129], v[26:33], v[196:203], v[126:129]
	v_mfma_f32_16x16x128_f8f6f4 v[122:125], v[18:25], v[196:203], v[122:125]
	v_mfma_f32_16x16x128_f8f6f4 v[106:109], v[18:25], v[204:211], v[106:109]
	v_mfma_f32_16x16x128_f8f6f4 v[110:113], v[26:33], v[204:211], v[110:113]
	s_setprio 0
	s_setprio 1
	v_mfma_f32_16x16x128_f8f6f4 v[102:105], v[10:17], v[204:211], v[102:105]
	v_mfma_f32_16x16x128_f8f6f4 v[98:101], v[2:9], v[204:211], v[98:101]
	v_mfma_f32_16x16x128_f8f6f4 v[146:149], v[2:9], v[174:181], v[146:149]
	v_mfma_f32_16x16x128_f8f6f4 v[150:153], v[10:17], v[174:181], v[150:153]
	v_mfma_f32_16x16x128_f8f6f4 v[134:137], v[10:17], v[188:195], v[134:137]
	v_mfma_f32_16x16x128_f8f6f4 v[130:133], v[2:9], v[188:195], v[130:133]
	v_mfma_f32_16x16x128_f8f6f4 v[114:117], v[2:9], v[196:203], v[114:117]
	v_mfma_f32_16x16x128_f8f6f4 v[118:121], v[10:17], v[196:203], v[118:121]
	s_setprio 0
	s_barrier
	s_add_i32 s24, s42, s3
	v_lshl_add_u64 v[174:175], s[28:29], 0, v[164:165]
	s_mov_b32 m0, s24
	ds_read_b128 v[188:191], v187 offset:16384
	ds_read_b128 v[192:195], v187 offset:17408
	ds_read_b128 v[196:199], v187 offset:18432
	ds_read_b128 v[200:203], v187 offset:19456
	ds_read_b128 v[204:207], v187 offset:20480
	ds_read_b128 v[208:211], v187 offset:21504
	ds_read_b128 v[212:215], v187 offset:22528
	ds_read_b128 v[216:219], v187 offset:23552
	global_load_lds_dwordx4 v[174:175], off
	s_add_i32 m0, s24, 0x2000
	s_add_u32 s24, s28, 0x158000
	v_lshl_add_u64 v[176:177], s[28:29], 0, v[162:163]
	s_addc_u32 s25, s29, 0
	s_add_i32 s59, s43, s3
	global_load_lds_dwordx4 v[176:177], off
	v_lshl_add_u64 v[178:179], s[24:25], 0, v[164:165]
	s_mov_b32 m0, s59
	v_lshl_add_u64 v[180:181], s[30:31], 0, v[162:163]
	global_load_lds_dwordx4 v[178:179], off
	v_lshl_add_u64 v[178:179], s[24:25], 0, v[162:163]
	s_add_i32 m0, s59, 0x2000
	s_nop 0
	global_load_lds_dwordx4 v[178:179], off
	v_lshl_add_u64 v[178:179], s[30:31], 0, v[164:165]
	s_mov_b32 m0, s7
	s_nop 0
	global_load_lds_dwordx4 v[178:179], off
	s_mov_b32 m0, s17
	s_nop 0
	global_load_lds_dwordx4 v[180:181], off
	s_waitcnt vmcnt(8)
	s_waitcnt lgkmcnt(0)
	s_barrier
	s_setprio 1
	s_waitcnt lgkmcnt(0)
	v_mfma_f32_16x16x128_f8f6f4 v[78:81], v[26:33], v[196:203], v[78:81]
	v_mfma_f32_16x16x128_f8f6f4 v[74:77], v[18:25], v[196:203], v[74:77]
	v_mfma_f32_16x16x128_f8f6f4 v[90:93], v[18:25], v[188:195], v[90:93]
	v_mfma_f32_16x16x128_f8f6f4 v[94:97], v[26:33], v[188:195], v[94:97]
	v_mfma_f32_16x16x128_f8f6f4 v[62:65], v[26:33], v[204:211], v[62:65]
	v_mfma_f32_16x16x128_f8f6f4 v[58:61], v[18:25], v[204:211], v[58:61]
	v_mfma_f32_16x16x128_f8f6f4 v[42:45], v[18:25], v[212:219], v[42:45]
	v_mfma_f32_16x16x128_f8f6f4 v[46:49], v[26:33], v[212:219], v[46:49]
	s_setprio 0
	s_setprio 1
	v_mfma_f32_16x16x128_f8f6f4 v[38:41], v[10:17], v[212:219], v[38:41]
	v_mfma_f32_16x16x128_f8f6f4 v[34:37], v[2:9], v[212:219], v[34:37]
	v_mfma_f32_16x16x128_f8f6f4 v[82:85], v[2:9], v[188:195], v[82:85]
	v_mfma_f32_16x16x128_f8f6f4 v[86:89], v[10:17], v[188:195], v[86:89]
	v_mfma_f32_16x16x128_f8f6f4 v[70:73], v[10:17], v[196:203], v[70:73]
	v_mfma_f32_16x16x128_f8f6f4 v[66:69], v[2:9], v[196:203], v[66:69]
	v_mfma_f32_16x16x128_f8f6f4 v[50:53], v[2:9], v[204:211], v[50:53]
	v_mfma_f32_16x16x128_f8f6f4 v[54:57], v[10:17], v[204:211], v[54:57]
	s_setprio 0
	s_barrier
	s_add_i32 s59, 0, 0x18000
	s_add_i32 s60, 0, 0x1c000
	v_add_u32_e32 v14, s59, v183
	v_add_u32_e32 v30, s60, v183
	ds_read_b128 v[2:5], v14
	ds_read_b128 v[6:9], v14 offset:1024
	ds_read_b128 v[10:13], v14 offset:2048
	ds_read_b128 v[14:17], v14 offset:3072
	ds_read_b128 v[18:21], v30
	ds_read_b128 v[22:25], v30 offset:1024
	ds_read_b128 v[26:29], v30 offset:2048
	ds_read_b128 v[30:33], v30 offset:3072
	s_add_u32 s24, s30, 0x158000
	s_addc_u32 s25, s31, 0
	s_mov_b32 m0, s34
	v_lshl_add_u64 v[220:221], s[24:25], 0, v[164:165]
	ds_read_b128 v[188:191], v187 offset:32768
	ds_read_b128 v[192:195], v187 offset:33792
	ds_read_b128 v[196:199], v187 offset:34816
	ds_read_b128 v[200:203], v187 offset:35840
	ds_read_b128 v[204:207], v187 offset:36864
	ds_read_b128 v[208:211], v187 offset:37888
	ds_read_b128 v[212:215], v187 offset:38912
	ds_read_b128 v[216:219], v187 offset:39936
	global_load_lds_dwordx4 v[220:221], off
	v_lshl_add_u64 v[220:221], s[24:25], 0, v[162:163]
	s_mov_b32 m0, s35
	s_nop 0
	global_load_lds_dwordx4 v[220:221], off
	s_waitcnt vmcnt(8)
	s_waitcnt lgkmcnt(0)
	s_barrier
	s_setprio 1
	s_waitcnt lgkmcnt(0)
	v_mfma_f32_16x16x128_f8f6f4 v[122:125], v[10:17], v[204:211], v[122:125]
	v_mfma_f32_16x16x128_f8f6f4 v[126:129], v[2:9], v[204:211], v[126:129]
	v_mfma_f32_16x16x128_f8f6f4 v[158:161], v[2:9], v[188:195], v[158:161]
	v_mfma_f32_16x16x128_f8f6f4 v[154:157], v[10:17], v[188:195], v[154:157]
	v_mfma_f32_16x16x128_f8f6f4 v[138:141], v[10:17], v[196:203], v[138:141]
	v_mfma_f32_16x16x128_f8f6f4 v[142:145], v[2:9], v[196:203], v[142:145]
	v_mfma_f32_16x16x128_f8f6f4 v[110:113], v[2:9], v[212:219], v[110:113]
	v_mfma_f32_16x16x128_f8f6f4 v[106:109], v[10:17], v[212:219], v[106:109]
	s_setprio 0
	s_setprio 1
	v_mfma_f32_16x16x128_f8f6f4 v[102:105], v[18:25], v[212:219], v[102:105]
	v_mfma_f32_16x16x128_f8f6f4 v[98:101], v[26:33], v[212:219], v[98:101]
	v_mfma_f32_16x16x128_f8f6f4 v[146:149], v[26:33], v[188:195], v[146:149]
	v_mfma_f32_16x16x128_f8f6f4 v[150:153], v[18:25], v[188:195], v[150:153]
	v_mfma_f32_16x16x128_f8f6f4 v[134:137], v[18:25], v[196:203], v[134:137]
	v_mfma_f32_16x16x128_f8f6f4 v[130:133], v[26:33], v[196:203], v[130:133]
	v_mfma_f32_16x16x128_f8f6f4 v[114:117], v[26:33], v[204:211], v[114:117]
	v_mfma_f32_16x16x128_f8f6f4 v[118:121], v[18:25], v[204:211], v[118:121]
	s_setprio 0
	s_barrier
	s_add_i32 s24, s59, s3
	v_lshl_add_u64 v[174:175], v[174:175], 0, s[12:13]
	s_mov_b32 m0, s24
	ds_read_b128 v[188:191], v187 offset:49152
	ds_read_b128 v[192:195], v187 offset:50176
	ds_read_b128 v[196:199], v187 offset:51200
	ds_read_b128 v[200:203], v187 offset:52224
	ds_read_b128 v[204:207], v187 offset:53248
	ds_read_b128 v[208:211], v187 offset:54272
	ds_read_b128 v[212:215], v187 offset:55296
	ds_read_b128 v[216:219], v187 offset:56320
	global_load_lds_dwordx4 v[174:175], off
	s_add_i32 m0, s24, 0x2000
	s_add_u32 s24, s28, 0x158080
	v_lshl_add_u64 v[174:175], v[176:177], 0, s[12:13]
	s_addc_u32 s25, s29, 0
	s_add_i32 s28, s60, s3
	global_load_lds_dwordx4 v[174:175], off
	v_lshl_add_u64 v[174:175], s[24:25], 0, v[164:165]
	s_mov_b32 m0, s28
	s_nop 0
	global_load_lds_dwordx4 v[174:175], off
	v_lshl_add_u64 v[174:175], s[24:25], 0, v[162:163]
	s_add_i32 m0, s28, 0x2000
	s_nop 0
	global_load_lds_dwordx4 v[174:175], off
	v_lshl_add_u64 v[174:175], v[178:179], 0, s[12:13]
	s_mov_b32 m0, s38
	s_nop 0
	global_load_lds_dwordx4 v[174:175], off
	v_lshl_add_u64 v[174:175], v[180:181], 0, s[12:13]
	s_mov_b32 m0, s39
	s_nop 0
	global_load_lds_dwordx4 v[174:175], off
	s_waitcnt vmcnt(8)
	s_waitcnt lgkmcnt(0)
	s_barrier
	s_setprio 1
	s_waitcnt lgkmcnt(0)
	v_mfma_f32_16x16x128_f8f6f4 v[62:65], v[2:9], v[204:211], v[62:65]
	v_mfma_f32_16x16x128_f8f6f4 v[58:61], v[10:17], v[204:211], v[58:61]
	v_mfma_f32_16x16x128_f8f6f4 v[90:93], v[10:17], v[188:195], v[90:93]
	v_mfma_f32_16x16x128_f8f6f4 v[94:97], v[2:9], v[188:195], v[94:97]
	v_mfma_f32_16x16x128_f8f6f4 v[78:81], v[2:9], v[196:203], v[78:81]
	v_mfma_f32_16x16x128_f8f6f4 v[74:77], v[10:17], v[196:203], v[74:77]
	v_mfma_f32_16x16x128_f8f6f4 v[42:45], v[10:17], v[212:219], v[42:45]
	v_mfma_f32_16x16x128_f8f6f4 v[46:49], v[2:9], v[212:219], v[46:49]
	s_setprio 0
	s_setprio 1
	v_mfma_f32_16x16x128_f8f6f4 v[38:41], v[18:25], v[212:219], v[38:41]
	v_mfma_f32_16x16x128_f8f6f4 v[34:37], v[26:33], v[212:219], v[34:37]
	v_mfma_f32_16x16x128_f8f6f4 v[82:85], v[26:33], v[188:195], v[82:85]
	v_mfma_f32_16x16x128_f8f6f4 v[86:89], v[18:25], v[188:195], v[86:89]
	v_mfma_f32_16x16x128_f8f6f4 v[70:73], v[18:25], v[196:203], v[70:73]
	v_mfma_f32_16x16x128_f8f6f4 v[66:69], v[26:33], v[196:203], v[66:69]
	v_mfma_f32_16x16x128_f8f6f4 v[50:53], v[26:33], v[204:211], v[50:53]
	v_mfma_f32_16x16x128_f8f6f4 v[54:57], v[18:25], v[204:211], v[54:57]
	s_setprio 0
	s_barrier
	s_add_i32 s58, s58, 2
	s_add_u32 s26, s26, 0x100
	s_addc_u32 s27, s27, 0
	s_add_u32 s50, s50, 0x100
	s_addc_u32 s51, s51, 0
	s_cmpk_gt_u32 s58, 0x53
	s_cbranch_scc0 .LBB0_318
	s_and_b64 vcc, exec, s[14:15]
	s_cbranch_vccz .LBB0_321
	s_barrier

.LBB0_1291:
	ds_read_b128 v[26:29], v184
	ds_read_b128 v[30:33], v184 offset:1024
	ds_read_b128 v[18:21], v184 offset:2048
	ds_read_b128 v[22:25], v184 offset:3072
	ds_read_b128 v[10:13], v185
	ds_read_b128 v[14:17], v185 offset:1024
	ds_read_b128 v[2:5], v185 offset:2048
	ds_read_b128 v[6:9], v185 offset:3072
	s_add_u32 s20, s14, s16
	s_addc_u32 s21, s15, s17
	s_add_u32 s20, s20, 0x2a800100
	s_addc_u32 s21, s21, 0
	s_add_u32 s48, s31, s16
	s_addc_u32 s49, s34, s17
	s_cmpk_eq_i32 s16, 0x700
	s_cselect_b32 s23, s9, s21
	s_cselect_b32 s22, s8, s20
	s_cselect_b32 s21, s5, s49
	s_cselect_b32 s20, s4, s48
	s_mov_b32 m0, s36
	v_lshl_add_u64 v[214:215], v[170:171], 0, s[16:17]
	ds_read_b128 v[174:177], v186
	ds_read_b128 v[178:181], v186 offset:1024
	ds_read_b128 v[190:193], v186 offset:2048
	ds_read_b128 v[194:197], v186 offset:3072
	ds_read_b128 v[198:201], v186 offset:4096
	ds_read_b128 v[202:205], v186 offset:5120
	ds_read_b128 v[206:209], v186 offset:6144
	ds_read_b128 v[210:213], v186 offset:7168
	global_load_lds_dwordx4 v[214:215], off
	v_lshl_add_u64 v[214:215], v[172:173], 0, s[16:17]
	s_mov_b32 m0, s37
	s_nop 0
	global_load_lds_dwordx4 v[214:215], off
	s_waitcnt vmcnt(8)
	s_waitcnt lgkmcnt(0)
	s_barrier
	s_setprio 1
	s_waitcnt lgkmcnt(0)
	v_mfma_f32_16x16x128_f8f6f4 v[158:161], v[26:33], v[174:181], v[158:161]
	v_mfma_f32_16x16x128_f8f6f4 v[154:157], v[18:25], v[174:181], v[154:157]
	v_mfma_f32_16x16x128_f8f6f4 v[138:141], v[18:25], v[190:197], v[138:141]
	v_mfma_f32_16x16x128_f8f6f4 v[146:149], v[26:33], v[190:197], v[146:149]
	v_mfma_f32_16x16x128_f8f6f4 v[130:133], v[26:33], v[198:205], v[130:133]
	v_mfma_f32_16x16x128_f8f6f4 v[122:125], v[18:25], v[198:205], v[122:125]
	v_mfma_f32_16x16x128_f8f6f4 v[106:109], v[18:25], v[206:213], v[106:109]
	v_mfma_f32_16x16x128_f8f6f4 v[114:117], v[26:33], v[206:213], v[114:117]
	s_setprio 0
	s_setprio 1
	v_mfma_f32_16x16x128_f8f6f4 v[102:105], v[10:17], v[206:213], v[102:105]
	v_mfma_f32_16x16x128_f8f6f4 v[98:101], v[2:9], v[206:213], v[98:101]
	v_mfma_f32_16x16x128_f8f6f4 v[142:145], v[2:9], v[174:181], v[142:145]
	v_mfma_f32_16x16x128_f8f6f4 v[150:153], v[10:17], v[174:181], v[150:153]
	v_mfma_f32_16x16x128_f8f6f4 v[134:137], v[10:17], v[190:197], v[134:137]
	v_mfma_f32_16x16x128_f8f6f4 v[126:129], v[2:9], v[190:197], v[126:129]
	v_mfma_f32_16x16x128_f8f6f4 v[110:113], v[2:9], v[198:205], v[110:113]
	v_mfma_f32_16x16x128_f8f6f4 v[118:121], v[10:17], v[198:205], v[118:121]
	s_setprio 0
	s_barrier
	s_mov_b32 m0, s38
	v_lshl_add_u64 v[174:175], s[20:21], 0, v[164:165]
	s_add_u32 s48, s20, 0x80000
	ds_read_b128 v[190:193], v186 offset:16384
	ds_read_b128 v[194:197], v186 offset:17408
	ds_read_b128 v[198:201], v186 offset:18432
	ds_read_b128 v[202:205], v186 offset:19456
	ds_read_b128 v[206:209], v186 offset:20480
	ds_read_b128 v[210:213], v186 offset:21504
	ds_read_b128 v[214:217], v186 offset:22528
	ds_read_b128 v[218:221], v186 offset:23552
	global_load_lds_dwordx4 v[174:175], off
	v_lshl_add_u64 v[176:177], s[20:21], 0, v[168:169]
	s_mov_b32 m0, s39
	s_addc_u32 s49, s21, 0
	global_load_lds_dwordx4 v[176:177], off
	v_lshl_add_u64 v[178:179], s[48:49], 0, v[164:165]
	s_mov_b32 m0, s40
	v_lshl_add_u64 v[180:181], s[22:23], 0, v[166:167]
	global_load_lds_dwordx4 v[178:179], off
	v_lshl_add_u64 v[178:179], s[48:49], 0, v[168:169]
	s_mov_b32 m0, s41
	s_nop 0
	global_load_lds_dwordx4 v[178:179], off
	v_lshl_add_u64 v[178:179], s[22:23], 0, v[162:163]
	s_mov_b32 m0, s24
	s_nop 0
	global_load_lds_dwordx4 v[178:179], off
	s_mov_b32 m0, s25
	s_nop 0
	global_load_lds_dwordx4 v[180:181], off
	s_waitcnt vmcnt(8)
	s_waitcnt lgkmcnt(0)
	s_barrier
	s_setprio 1
	s_waitcnt lgkmcnt(0)
	v_mfma_f32_16x16x128_f8f6f4 v[82:85], v[26:33], v[198:205], v[82:85]
	v_mfma_f32_16x16x128_f8f6f4 v[74:77], v[18:25], v[198:205], v[74:77]
	v_mfma_f32_16x16x128_f8f6f4 v[90:93], v[18:25], v[190:197], v[90:93]
	v_mfma_f32_16x16x128_f8f6f4 v[94:97], v[26:33], v[190:197], v[94:97]
	v_mfma_f32_16x16x128_f8f6f4 v[66:69], v[26:33], v[206:213], v[66:69]
	v_mfma_f32_16x16x128_f8f6f4 v[58:61], v[18:25], v[206:213], v[58:61]
	v_mfma_f32_16x16x128_f8f6f4 v[42:45], v[18:25], v[214:221], v[42:45]
	v_mfma_f32_16x16x128_f8f6f4 v[50:53], v[26:33], v[214:221], v[50:53]
	s_setprio 0
	s_setprio 1
	v_mfma_f32_16x16x128_f8f6f4 v[38:41], v[10:17], v[214:221], v[38:41]
	v_mfma_f32_16x16x128_f8f6f4 v[34:37], v[2:9], v[214:221], v[34:37]
	v_mfma_f32_16x16x128_f8f6f4 v[78:81], v[2:9], v[190:197], v[78:81]
	v_mfma_f32_16x16x128_f8f6f4 v[86:89], v[10:17], v[190:197], v[86:89]
	v_mfma_f32_16x16x128_f8f6f4 v[70:73], v[10:17], v[198:205], v[70:73]
	v_mfma_f32_16x16x128_f8f6f4 v[62:65], v[2:9], v[198:205], v[62:65]
	v_mfma_f32_16x16x128_f8f6f4 v[46:49], v[2:9], v[206:213], v[46:49]
	v_mfma_f32_16x16x128_f8f6f4 v[54:57], v[10:17], v[206:213], v[54:57]
	s_setprio 0
	s_barrier
	ds_read_b128 v[2:5], v187
	ds_read_b128 v[6:9], v187 offset:1024
	ds_read_b128 v[10:13], v187 offset:2048
	ds_read_b128 v[14:17], v187 offset:3072
	ds_read_b128 v[18:21], v188
	ds_read_b128 v[22:25], v188 offset:1024
	ds_read_b128 v[26:29], v188 offset:2048
	ds_read_b128 v[30:33], v188 offset:3072
	s_add_u32 s22, s22, 0x80000
	s_addc_u32 s23, s23, 0
	s_mov_b32 m0, s26
	v_lshl_add_u64 v[222:223], s[22:23], 0, v[162:163]
	ds_read_b128 v[190:193], v186 offset:32768
	ds_read_b128 v[194:197], v186 offset:33792
	ds_read_b128 v[198:201], v186 offset:34816
	ds_read_b128 v[202:205], v186 offset:35840
	ds_read_b128 v[206:209], v186 offset:36864
	ds_read_b128 v[210:213], v186 offset:37888
	ds_read_b128 v[214:217], v186 offset:38912
	ds_read_b128 v[218:221], v186 offset:39936
	global_load_lds_dwordx4 v[222:223], off
	v_lshl_add_u64 v[222:223], s[22:23], 0, v[166:167]
	s_mov_b32 m0, s27
	s_nop 0
	global_load_lds_dwordx4 v[222:223], off
	s_waitcnt vmcnt(8)
	s_waitcnt lgkmcnt(0)
	s_barrier
	s_setprio 1
	s_waitcnt lgkmcnt(0)
	v_mfma_f32_16x16x128_f8f6f4 v[122:125], v[10:17], v[206:213], v[122:125]
	v_mfma_f32_16x16x128_f8f6f4 v[130:133], v[2:9], v[206:213], v[130:133]
	v_mfma_f32_16x16x128_f8f6f4 v[158:161], v[2:9], v[190:197], v[158:161]
	v_mfma_f32_16x16x128_f8f6f4 v[154:157], v[10:17], v[190:197], v[154:157]
	v_mfma_f32_16x16x128_f8f6f4 v[138:141], v[10:17], v[198:205], v[138:141]
	v_mfma_f32_16x16x128_f8f6f4 v[146:149], v[2:9], v[198:205], v[146:149]
	v_mfma_f32_16x16x128_f8f6f4 v[114:117], v[2:9], v[214:221], v[114:117]
	v_mfma_f32_16x16x128_f8f6f4 v[106:109], v[10:17], v[214:221], v[106:109]
	s_setprio 0
	s_setprio 1
	v_mfma_f32_16x16x128_f8f6f4 v[102:105], v[18:25], v[214:221], v[102:105]
	v_mfma_f32_16x16x128_f8f6f4 v[98:101], v[26:33], v[214:221], v[98:101]
	v_mfma_f32_16x16x128_f8f6f4 v[142:145], v[26:33], v[190:197], v[142:145]
	v_mfma_f32_16x16x128_f8f6f4 v[150:153], v[18:25], v[190:197], v[150:153]
	v_mfma_f32_16x16x128_f8f6f4 v[134:137], v[18:25], v[198:205], v[134:137]
	v_mfma_f32_16x16x128_f8f6f4 v[126:129], v[26:33], v[198:205], v[126:129]
	v_mfma_f32_16x16x128_f8f6f4 v[110:113], v[26:33], v[206:213], v[110:113]
	v_mfma_f32_16x16x128_f8f6f4 v[118:121], v[18:25], v[206:213], v[118:121]
	s_setprio 0
	s_barrier
	s_mov_b32 m0, s42
	v_lshl_add_u64 v[174:175], v[174:175], 0, s[12:13]
	s_add_u32 s20, s20, 0x80080
	ds_read_b128 v[190:193], v186 offset:49152
	ds_read_b128 v[194:197], v186 offset:50176
	ds_read_b128 v[198:201], v186 offset:51200
	ds_read_b128 v[202:205], v186 offset:52224
	ds_read_b128 v[206:209], v186 offset:53248
	ds_read_b128 v[210:213], v186 offset:54272
	ds_read_b128 v[214:217], v186 offset:55296
	ds_read_b128 v[218:221], v186 offset:56320
	global_load_lds_dwordx4 v[174:175], off
	v_lshl_add_u64 v[174:175], v[176:177], 0, s[12:13]
	s_mov_b32 m0, s43
	s_addc_u32 s21, s21, 0
	global_load_lds_dwordx4 v[174:175], off
	v_lshl_add_u64 v[174:175], s[20:21], 0, v[164:165]
	s_mov_b32 m0, s44
	s_nop 0
	global_load_lds_dwordx4 v[174:175], off
	v_lshl_add_u64 v[174:175], s[20:21], 0, v[168:169]
	s_mov_b32 m0, s45
	s_nop 0
	global_load_lds_dwordx4 v[174:175], off
	v_lshl_add_u64 v[174:175], v[178:179], 0, s[12:13]
	s_mov_b32 m0, s29
	s_nop 0
	global_load_lds_dwordx4 v[174:175], off
	v_lshl_add_u64 v[174:175], v[180:181], 0, s[12:13]
	s_mov_b32 m0, s30
	s_nop 0
	global_load_lds_dwordx4 v[174:175], off
	s_waitcnt vmcnt(8)
	s_waitcnt lgkmcnt(0)
	s_barrier
	s_setprio 1
	s_waitcnt lgkmcnt(0)
	v_mfma_f32_16x16x128_f8f6f4 v[66:69], v[2:9], v[206:213], v[66:69]
	v_mfma_f32_16x16x128_f8f6f4 v[58:61], v[10:17], v[206:213], v[58:61]
	v_mfma_f32_16x16x128_f8f6f4 v[90:93], v[10:17], v[190:197], v[90:93]
	v_mfma_f32_16x16x128_f8f6f4 v[94:97], v[2:9], v[190:197], v[94:97]
	v_mfma_f32_16x16x128_f8f6f4 v[82:85], v[2:9], v[198:205], v[82:85]
	v_mfma_f32_16x16x128_f8f6f4 v[74:77], v[10:17], v[198:205], v[74:77]
	v_mfma_f32_16x16x128_f8f6f4 v[42:45], v[10:17], v[214:221], v[42:45]
	v_mfma_f32_16x16x128_f8f6f4 v[50:53], v[2:9], v[214:221], v[50:53]
	s_setprio 0
	s_setprio 1
	v_mfma_f32_16x16x128_f8f6f4 v[38:41], v[18:25], v[214:221], v[38:41]
	v_mfma_f32_16x16x128_f8f6f4 v[34:37], v[26:33], v[214:221], v[34:37]
	v_mfma_f32_16x16x128_f8f6f4 v[78:81], v[26:33], v[190:197], v[78:81]
	v_mfma_f32_16x16x128_f8f6f4 v[86:89], v[18:25], v[190:197], v[86:89]
	v_mfma_f32_16x16x128_f8f6f4 v[70:73], v[18:25], v[198:205], v[70:73]
	v_mfma_f32_16x16x128_f8f6f4 v[62:65], v[26:33], v[198:205], v[62:65]
	v_mfma_f32_16x16x128_f8f6f4 v[46:49], v[26:33], v[206:213], v[46:49]
	v_mfma_f32_16x16x128_f8f6f4 v[54:57], v[18:25], v[206:213], v[54:57]
	s_setprio 0
	s_barrier
	s_add_i32 s35, s35, 2
	s_add_u32 s16, s16, 0x100
	s_addc_u32 s17, s17, 0
	s_cmp_gt_u32 s35, 13
	s_cbranch_scc0 .LBB0_1291
	s_cmpk_lt_u32 s19, 0x100
	s_cbranch_scc0 .LBB0_1294
	s_barrier

.LBB0_1309:
	ds_read_b128 v[26:29], v189
	ds_read_b128 v[30:33], v189 offset:1024
	ds_read_b128 v[18:21], v189 offset:2048
	ds_read_b128 v[22:25], v189 offset:3072
	ds_read_b128 v[10:13], v190
	ds_read_b128 v[14:17], v190 offset:1024
	ds_read_b128 v[2:5], v190 offset:2048
	ds_read_b128 v[6:9], v190 offset:3072
	s_add_u32 s40, s38, 0xfff80080
	s_addc_u32 s41, s39, -1
	s_cmp_eq_u32 s72, 28
	s_cselect_b32 s43, s18, s41
	s_cselect_b32 s42, s19, s40
	s_cselect_b32 s41, s27, s71
	s_cselect_b32 s40, s29, s70
	v_lshl_add_u64 v[216:217], s[38:39], 0, v[170:171]
	s_add_i32 m0, s37, 0xc000
	ds_read_b128 v[178:181], v191
	ds_read_b128 v[182:185], v191 offset:1024
	ds_read_b128 v[192:195], v191 offset:2048
	ds_read_b128 v[196:199], v191 offset:3072
	ds_read_b128 v[200:203], v191 offset:4096
	ds_read_b128 v[204:207], v191 offset:5120
	ds_read_b128 v[208:211], v191 offset:6144
	ds_read_b128 v[212:215], v191 offset:7168
	global_load_lds_dwordx4 v[216:217], off
	v_lshl_add_u64 v[216:217], s[38:39], 0, v[172:173]
	s_add_i32 m0, s37, 0xe000
	s_nop 0
	global_load_lds_dwordx4 v[216:217], off
	s_waitcnt vmcnt(8)
	s_waitcnt lgkmcnt(0)
	s_barrier
	s_setprio 1
	s_waitcnt lgkmcnt(0)
	v_mfma_f32_16x16x128_f8f6f4 v[158:161], v[26:33], v[178:185], v[158:161]
	v_mfma_f32_16x16x128_f8f6f4 v[154:157], v[18:25], v[178:185], v[154:157]
	v_mfma_f32_16x16x128_f8f6f4 v[138:141], v[18:25], v[192:199], v[138:141]
	v_mfma_f32_16x16x128_f8f6f4 v[146:149], v[26:33], v[192:199], v[146:149]
	v_mfma_f32_16x16x128_f8f6f4 v[130:133], v[26:33], v[200:207], v[130:133]
	v_mfma_f32_16x16x128_f8f6f4 v[122:125], v[18:25], v[200:207], v[122:125]
	v_mfma_f32_16x16x128_f8f6f4 v[106:109], v[18:25], v[208:215], v[106:109]
	v_mfma_f32_16x16x128_f8f6f4 v[114:117], v[26:33], v[208:215], v[114:117]
	s_setprio 0
	s_setprio 1
	v_mfma_f32_16x16x128_f8f6f4 v[102:105], v[10:17], v[208:215], v[102:105]
	v_mfma_f32_16x16x128_f8f6f4 v[98:101], v[2:9], v[208:215], v[98:101]
	v_mfma_f32_16x16x128_f8f6f4 v[142:145], v[2:9], v[178:185], v[142:145]
	v_mfma_f32_16x16x128_f8f6f4 v[150:153], v[10:17], v[178:185], v[150:153]
	v_mfma_f32_16x16x128_f8f6f4 v[134:137], v[10:17], v[192:199], v[134:137]
	v_mfma_f32_16x16x128_f8f6f4 v[126:129], v[2:9], v[192:199], v[126:129]
	v_mfma_f32_16x16x128_f8f6f4 v[110:113], v[2:9], v[200:207], v[110:113]
	v_mfma_f32_16x16x128_f8f6f4 v[118:121], v[10:17], v[200:207], v[118:121]
	s_setprio 0
	s_barrier
	s_add_i32 s64, s59, s3
	v_lshl_add_u64 v[178:179], s[40:41], 0, v[166:167]
	s_mov_b32 m0, s64
	ds_read_b128 v[192:195], v191 offset:16384
	ds_read_b128 v[196:199], v191 offset:17408
	ds_read_b128 v[200:203], v191 offset:18432
	ds_read_b128 v[204:207], v191 offset:19456
	ds_read_b128 v[208:211], v191 offset:20480
	ds_read_b128 v[212:215], v191 offset:21504
	ds_read_b128 v[216:219], v191 offset:22528
	ds_read_b128 v[220:223], v191 offset:23552
	global_load_lds_dwordx4 v[178:179], off
	s_add_i32 m0, s64, 0x2000
	s_add_u32 s64, s40, 0x80000
	v_lshl_add_u64 v[180:181], s[40:41], 0, v[162:163]
	s_addc_u32 s65, s41, 0
	s_add_i32 s73, s62, s3
	global_load_lds_dwordx4 v[180:181], off
	v_lshl_add_u64 v[182:183], s[64:65], 0, v[166:167]
	s_mov_b32 m0, s73
	v_lshl_add_u64 v[184:185], s[42:43], 0, v[164:165]
	global_load_lds_dwordx4 v[182:183], off
	v_lshl_add_u64 v[182:183], s[64:65], 0, v[162:163]
	s_add_i32 m0, s73, 0x2000
	s_nop 0
	global_load_lds_dwordx4 v[182:183], off
	v_lshl_add_u64 v[182:183], s[42:43], 0, v[168:169]
	s_mov_b32 m0, s37
	s_nop 0
	global_load_lds_dwordx4 v[182:183], off
	s_mov_b32 m0, s44
	s_nop 0
	global_load_lds_dwordx4 v[184:185], off
	s_waitcnt vmcnt(8)
	s_waitcnt lgkmcnt(0)
	s_barrier
	s_setprio 1
	s_waitcnt lgkmcnt(0)
	v_mfma_f32_16x16x128_f8f6f4 v[82:85], v[26:33], v[200:207], v[82:85]
	v_mfma_f32_16x16x128_f8f6f4 v[74:77], v[18:25], v[200:207], v[74:77]
	v_mfma_f32_16x16x128_f8f6f4 v[90:93], v[18:25], v[192:199], v[90:93]
	v_mfma_f32_16x16x128_f8f6f4 v[94:97], v[26:33], v[192:199], v[94:97]
	v_mfma_f32_16x16x128_f8f6f4 v[66:69], v[26:33], v[208:215], v[66:69]
	v_mfma_f32_16x16x128_f8f6f4 v[58:61], v[18:25], v[208:215], v[58:61]
	v_mfma_f32_16x16x128_f8f6f4 v[42:45], v[18:25], v[216:223], v[42:45]
	v_mfma_f32_16x16x128_f8f6f4 v[50:53], v[26:33], v[216:223], v[50:53]
	s_setprio 0
	s_setprio 1
	v_mfma_f32_16x16x128_f8f6f4 v[38:41], v[10:17], v[216:223], v[38:41]
	v_mfma_f32_16x16x128_f8f6f4 v[34:37], v[2:9], v[216:223], v[34:37]
	v_mfma_f32_16x16x128_f8f6f4 v[78:81], v[2:9], v[192:199], v[78:81]
	v_mfma_f32_16x16x128_f8f6f4 v[86:89], v[10:17], v[192:199], v[86:89]
	v_mfma_f32_16x16x128_f8f6f4 v[70:73], v[10:17], v[200:207], v[70:73]
	v_mfma_f32_16x16x128_f8f6f4 v[62:65], v[2:9], v[200:207], v[62:65]
	v_mfma_f32_16x16x128_f8f6f4 v[46:49], v[2:9], v[208:215], v[46:49]
	v_mfma_f32_16x16x128_f8f6f4 v[54:57], v[10:17], v[208:215], v[54:57]
	s_setprio 0
	s_barrier
	s_add_i32 s64, 0, 0x18000
	s_add_i32 s65, 0, 0x1c000
	v_add_u32_e32 v14, s64, v187
	v_add_u32_e32 v30, s65, v187
	ds_read_b128 v[2:5], v14
	ds_read_b128 v[6:9], v14 offset:1024
	ds_read_b128 v[10:13], v14 offset:2048
	ds_read_b128 v[14:17], v14 offset:3072
	ds_read_b128 v[18:21], v30
	ds_read_b128 v[22:25], v30 offset:1024
	ds_read_b128 v[26:29], v30 offset:2048
	ds_read_b128 v[30:33], v30 offset:3072
	s_add_u32 s42, s42, 0x80000
	s_addc_u32 s43, s43, 0
	s_mov_b32 m0, s45
	v_lshl_add_u64 v[224:225], s[42:43], 0, v[168:169]
	ds_read_b128 v[192:195], v191 offset:32768
	ds_read_b128 v[196:199], v191 offset:33792
	ds_read_b128 v[200:203], v191 offset:34816
	ds_read_b128 v[204:207], v191 offset:35840
	ds_read_b128 v[208:211], v191 offset:36864
	ds_read_b128 v[212:215], v191 offset:37888
	ds_read_b128 v[216:219], v191 offset:38912
	ds_read_b128 v[220:223], v191 offset:39936
	global_load_lds_dwordx4 v[224:225], off
	v_lshl_add_u64 v[224:225], s[42:43], 0, v[164:165]
	s_mov_b32 m0, s48
	s_nop 0
	global_load_lds_dwordx4 v[224:225], off
	s_waitcnt vmcnt(8)
	s_waitcnt lgkmcnt(0)
	s_barrier
	s_setprio 1
	s_waitcnt lgkmcnt(0)
	v_mfma_f32_16x16x128_f8f6f4 v[122:125], v[10:17], v[208:215], v[122:125]
	v_mfma_f32_16x16x128_f8f6f4 v[130:133], v[2:9], v[208:215], v[130:133]
	v_mfma_f32_16x16x128_f8f6f4 v[158:161], v[2:9], v[192:199], v[158:161]
	v_mfma_f32_16x16x128_f8f6f4 v[154:157], v[10:17], v[192:199], v[154:157]
	v_mfma_f32_16x16x128_f8f6f4 v[138:141], v[10:17], v[200:207], v[138:141]
	v_mfma_f32_16x16x128_f8f6f4 v[146:149], v[2:9], v[200:207], v[146:149]
	v_mfma_f32_16x16x128_f8f6f4 v[114:117], v[2:9], v[216:223], v[114:117]
	v_mfma_f32_16x16x128_f8f6f4 v[106:109], v[10:17], v[216:223], v[106:109]
	s_setprio 0
	s_setprio 1
	v_mfma_f32_16x16x128_f8f6f4 v[102:105], v[18:25], v[216:223], v[102:105]
	v_mfma_f32_16x16x128_f8f6f4 v[98:101], v[26:33], v[216:223], v[98:101]
	v_mfma_f32_16x16x128_f8f6f4 v[142:145], v[26:33], v[192:199], v[142:145]
	v_mfma_f32_16x16x128_f8f6f4 v[150:153], v[18:25], v[192:199], v[150:153]
	v_mfma_f32_16x16x128_f8f6f4 v[134:137], v[18:25], v[200:207], v[134:137]
	v_mfma_f32_16x16x128_f8f6f4 v[126:129], v[26:33], v[200:207], v[126:129]
	v_mfma_f32_16x16x128_f8f6f4 v[110:113], v[26:33], v[208:215], v[110:113]
	v_mfma_f32_16x16x128_f8f6f4 v[118:121], v[18:25], v[208:215], v[118:121]
	s_setprio 0
	s_barrier
	s_add_i32 s42, s64, s3
	v_lshl_add_u64 v[178:179], v[178:179], 0, s[12:13]
	s_mov_b32 m0, s42
	ds_read_b128 v[192:195], v191 offset:49152
	ds_read_b128 v[196:199], v191 offset:50176
	ds_read_b128 v[200:203], v191 offset:51200
	ds_read_b128 v[204:207], v191 offset:52224
	ds_read_b128 v[208:211], v191 offset:53248
	ds_read_b128 v[212:215], v191 offset:54272
	ds_read_b128 v[216:219], v191 offset:55296
	ds_read_b128 v[220:223], v191 offset:56320
	global_load_lds_dwordx4 v[178:179], off
	s_add_i32 m0, s42, 0x2000
	s_add_u32 s40, s40, 0x80080
	v_lshl_add_u64 v[178:179], v[180:181], 0, s[12:13]
	s_addc_u32 s41, s41, 0
	s_add_i32 s42, s65, s3
	global_load_lds_dwordx4 v[178:179], off
	v_lshl_add_u64 v[178:179], s[40:41], 0, v[166:167]
	s_mov_b32 m0, s42
	s_nop 0
	global_load_lds_dwordx4 v[178:179], off
	v_lshl_add_u64 v[178:179], s[40:41], 0, v[162:163]
	s_add_i32 m0, s42, 0x2000
	s_nop 0
	global_load_lds_dwordx4 v[178:179], off
	v_lshl_add_u64 v[178:179], v[182:183], 0, s[12:13]
	s_mov_b32 m0, s51
	s_nop 0
	global_load_lds_dwordx4 v[178:179], off
	v_lshl_add_u64 v[178:179], v[184:185], 0, s[12:13]
	s_mov_b32 m0, s58
	s_nop 0
	global_load_lds_dwordx4 v[178:179], off
	s_waitcnt vmcnt(8)
	s_waitcnt lgkmcnt(0)
	s_barrier
	s_setprio 1
	s_waitcnt lgkmcnt(0)
	v_mfma_f32_16x16x128_f8f6f4 v[66:69], v[2:9], v[208:215], v[66:69]
	v_mfma_f32_16x16x128_f8f6f4 v[58:61], v[10:17], v[208:215], v[58:61]
	v_mfma_f32_16x16x128_f8f6f4 v[90:93], v[10:17], v[192:199], v[90:93]
	v_mfma_f32_16x16x128_f8f6f4 v[94:97], v[2:9], v[192:199], v[94:97]
	v_mfma_f32_16x16x128_f8f6f4 v[82:85], v[2:9], v[200:207], v[82:85]
	v_mfma_f32_16x16x128_f8f6f4 v[74:77], v[10:17], v[200:207], v[74:77]
	v_mfma_f32_16x16x128_f8f6f4 v[42:45], v[10:17], v[216:223], v[42:45]
	v_mfma_f32_16x16x128_f8f6f4 v[50:53], v[2:9], v[216:223], v[50:53]
	s_setprio 0
	s_setprio 1
	v_mfma_f32_16x16x128_f8f6f4 v[38:41], v[18:25], v[216:223], v[38:41]
	v_mfma_f32_16x16x128_f8f6f4 v[34:37], v[26:33], v[216:223], v[34:37]
	v_mfma_f32_16x16x128_f8f6f4 v[78:81], v[26:33], v[192:199], v[78:81]
	v_mfma_f32_16x16x128_f8f6f4 v[86:89], v[18:25], v[192:199], v[86:89]
	v_mfma_f32_16x16x128_f8f6f4 v[70:73], v[18:25], v[200:207], v[70:73]
	v_mfma_f32_16x16x128_f8f6f4 v[62:65], v[26:33], v[200:207], v[62:65]
	v_mfma_f32_16x16x128_f8f6f4 v[46:49], v[26:33], v[208:215], v[46:49]
	v_mfma_f32_16x16x128_f8f6f4 v[54:57], v[18:25], v[208:215], v[54:57]
	s_setprio 0
	s_barrier
	s_add_i32 s72, s72, 2
	s_add_u32 s38, s38, 0x100
	s_addc_u32 s39, s39, 0
	s_add_u32 s70, s70, 0x100
	s_addc_u32 s71, s71, 0
	s_cmp_gt_u32 s72, 29
	s_cbranch_scc0 .LBB0_1309
	s_and_b64 vcc, exec, s[14:15]
	s_cbranch_vccz .LBB0_1312
	s_barrier

.LBB0_1558:
	s_add_u32 s39, s30, s38
	s_addc_u32 s44, s31, 0
	s_add_u32 s42, s39, 0x100
	s_addc_u32 s43, s44, 0
	s_and_b64 s[40:41], s[36:37], exec
	s_cselect_b32 s41, s18, s43
	s_cselect_b32 s40, s19, s42
	s_add_u32 s38, s28, s38
	s_addc_u32 s42, s29, 0
	s_add_u32 s38, s38, 0x100
	s_addc_u32 s42, s42, 0
	s_and_b64 s[36:37], s[36:37], exec
	s_cselect_b32 s43, s17, s42
	s_cselect_b32 s42, s21, s38
	s_add_u32 s76, s39, 0x10080
	ds_read_b128 v[26:29], v181
	ds_read_b128 v[30:33], v181 offset:1024
	ds_read_b128 v[18:21], v181 offset:2048
	ds_read_b128 v[22:25], v181 offset:3072
	ds_read_b128 v[10:13], v182
	ds_read_b128 v[14:17], v182 offset:1024
	ds_read_b128 v[2:5], v182 offset:2048
	ds_read_b128 v[6:9], v182 offset:3072
	s_addc_u32 s77, s44, 0
	s_add_i32 s75, s63, s15
	s_add_i32 m0, s27, 0xc000
	s_add_i32 s78, s27, 0xe000
	s_add_i32 s72, s75, 0x2000
	s_add_u32 s44, s42, 0x10000
	s_addc_u32 s45, s43, 0
	s_add_i32 s74, s64, s15
	s_add_i32 s73, s74, 0x2000
	s_add_i32 s71, 0, 0x18000
	s_add_i32 s70, 0, 0x1c000
	s_add_u32 s38, s40, 0x10000
	s_addc_u32 s39, s41, 0
	s_add_i32 s69, s71, s15
	s_add_i32 s67, s69, 0x2000
	s_add_u32 s36, s42, 0x10080
	s_addc_u32 s37, s43, 0
	s_add_i32 s68, s70, s15
	s_add_i32 s66, s68, 0x2000
	v_lshl_add_u64 v[208:209], s[76:77], 0, v[164:165]
	ds_read_b128 v[170:173], v183
	ds_read_b128 v[174:177], v183 offset:1024
	ds_read_b128 v[184:187], v183 offset:2048
	ds_read_b128 v[188:191], v183 offset:3072
	ds_read_b128 v[192:195], v183 offset:4096
	ds_read_b128 v[196:199], v183 offset:5120
	ds_read_b128 v[200:203], v183 offset:6144
	ds_read_b128 v[204:207], v183 offset:7168
	global_load_lds_dwordx4 v[208:209], off
	v_lshl_add_u64 v[208:209], s[76:77], 0, v[162:163]
	s_mov_b32 m0, s78
	s_nop 0
	global_load_lds_dwordx4 v[208:209], off
	s_waitcnt vmcnt(8)
	s_waitcnt lgkmcnt(0)
	s_barrier
	s_setprio 1
	s_waitcnt lgkmcnt(0)
	v_mfma_f32_16x16x128_f8f6f4 v[158:161], v[26:33], v[170:177], v[158:161]
	v_mfma_f32_16x16x128_f8f6f4 v[154:157], v[18:25], v[170:177], v[154:157]
	v_mfma_f32_16x16x128_f8f6f4 v[138:141], v[18:25], v[184:191], v[138:141]
	v_mfma_f32_16x16x128_f8f6f4 v[142:145], v[26:33], v[184:191], v[142:145]
	v_mfma_f32_16x16x128_f8f6f4 v[126:129], v[26:33], v[192:199], v[126:129]
	v_mfma_f32_16x16x128_f8f6f4 v[122:125], v[18:25], v[192:199], v[122:125]
	v_mfma_f32_16x16x128_f8f6f4 v[106:109], v[18:25], v[200:207], v[106:109]
	v_mfma_f32_16x16x128_f8f6f4 v[110:113], v[26:33], v[200:207], v[110:113]
	s_setprio 0
	s_setprio 1
	v_mfma_f32_16x16x128_f8f6f4 v[102:105], v[10:17], v[200:207], v[102:105]
	v_mfma_f32_16x16x128_f8f6f4 v[98:101], v[2:9], v[200:207], v[98:101]
	v_mfma_f32_16x16x128_f8f6f4 v[146:149], v[2:9], v[170:177], v[146:149]
	v_mfma_f32_16x16x128_f8f6f4 v[150:153], v[10:17], v[170:177], v[150:153]
	v_mfma_f32_16x16x128_f8f6f4 v[134:137], v[10:17], v[184:191], v[134:137]
	v_mfma_f32_16x16x128_f8f6f4 v[130:133], v[2:9], v[184:191], v[130:133]
	v_mfma_f32_16x16x128_f8f6f4 v[114:117], v[2:9], v[192:199], v[114:117]
	v_mfma_f32_16x16x128_f8f6f4 v[118:121], v[10:17], v[192:199], v[118:121]
	s_setprio 0
	s_barrier
	s_mov_b32 m0, s75
	v_lshl_add_u64 v[170:171], s[42:43], 0, v[164:165]
	ds_read_b128 v[184:187], v183 offset:16384
	ds_read_b128 v[188:191], v183 offset:17408
	ds_read_b128 v[192:195], v183 offset:18432
	ds_read_b128 v[196:199], v183 offset:19456
	ds_read_b128 v[200:203], v183 offset:20480
	ds_read_b128 v[204:207], v183 offset:21504
	ds_read_b128 v[208:211], v183 offset:22528
	ds_read_b128 v[212:215], v183 offset:23552
	global_load_lds_dwordx4 v[170:171], off
	v_lshl_add_u64 v[172:173], s[42:43], 0, v[162:163]
	s_mov_b32 m0, s72
	v_lshl_add_u64 v[174:175], s[44:45], 0, v[164:165]
	global_load_lds_dwordx4 v[172:173], off
	s_mov_b32 m0, s74
	v_lshl_add_u64 v[176:177], s[40:41], 0, v[162:163]
	global_load_lds_dwordx4 v[174:175], off
	v_lshl_add_u64 v[174:175], s[44:45], 0, v[162:163]
	s_mov_b32 m0, s73
	s_nop 0
	global_load_lds_dwordx4 v[174:175], off
	v_lshl_add_u64 v[174:175], s[40:41], 0, v[164:165]
	s_mov_b32 m0, s27
	s_nop 0
	global_load_lds_dwordx4 v[174:175], off
	s_mov_b32 m0, s49
	s_nop 0
	global_load_lds_dwordx4 v[176:177], off
	s_waitcnt vmcnt(8)
	s_waitcnt lgkmcnt(0)
	s_barrier
	s_setprio 1
	s_waitcnt lgkmcnt(0)
	v_mfma_f32_16x16x128_f8f6f4 v[78:81], v[26:33], v[192:199], v[78:81]
	v_mfma_f32_16x16x128_f8f6f4 v[74:77], v[18:25], v[192:199], v[74:77]
	v_mfma_f32_16x16x128_f8f6f4 v[90:93], v[18:25], v[184:191], v[90:93]
	v_mfma_f32_16x16x128_f8f6f4 v[94:97], v[26:33], v[184:191], v[94:97]
	v_mfma_f32_16x16x128_f8f6f4 v[62:65], v[26:33], v[200:207], v[62:65]
	v_mfma_f32_16x16x128_f8f6f4 v[58:61], v[18:25], v[200:207], v[58:61]
	v_mfma_f32_16x16x128_f8f6f4 v[42:45], v[18:25], v[208:215], v[42:45]
	v_mfma_f32_16x16x128_f8f6f4 v[54:57], v[26:33], v[208:215], v[54:57]
	s_setprio 0
	s_setprio 1
	v_mfma_f32_16x16x128_f8f6f4 v[38:41], v[10:17], v[208:215], v[38:41]
	v_mfma_f32_16x16x128_f8f6f4 v[34:37], v[2:9], v[208:215], v[34:37]
	v_mfma_f32_16x16x128_f8f6f4 v[82:85], v[2:9], v[184:191], v[82:85]
	v_mfma_f32_16x16x128_f8f6f4 v[86:89], v[10:17], v[184:191], v[86:89]
	v_mfma_f32_16x16x128_f8f6f4 v[70:73], v[10:17], v[192:199], v[70:73]
	v_mfma_f32_16x16x128_f8f6f4 v[66:69], v[2:9], v[192:199], v[66:69]
	v_mfma_f32_16x16x128_f8f6f4 v[46:49], v[2:9], v[200:207], v[46:49]
	v_mfma_f32_16x16x128_f8f6f4 v[50:53], v[10:17], v[200:207], v[50:53]
	s_setprio 0
	s_barrier
	v_add_u32_e32 v14, s71, v179
	v_add_u32_e32 v30, s70, v179
	ds_read_b128 v[2:5], v14
	ds_read_b128 v[6:9], v14 offset:1024
	ds_read_b128 v[10:13], v14 offset:2048
	ds_read_b128 v[14:17], v14 offset:3072
	ds_read_b128 v[18:21], v30
	ds_read_b128 v[22:25], v30 offset:1024
	ds_read_b128 v[26:29], v30 offset:2048
	ds_read_b128 v[30:33], v30 offset:3072
	s_mov_b32 m0, s50
	v_lshl_add_u64 v[216:217], s[38:39], 0, v[164:165]
	ds_read_b128 v[184:187], v183 offset:32768
	ds_read_b128 v[188:191], v183 offset:33792
	ds_read_b128 v[192:195], v183 offset:34816
	ds_read_b128 v[196:199], v183 offset:35840
	ds_read_b128 v[200:203], v183 offset:36864
	ds_read_b128 v[204:207], v183 offset:37888
	ds_read_b128 v[208:211], v183 offset:38912
	ds_read_b128 v[212:215], v183 offset:39936
	global_load_lds_dwordx4 v[216:217], off
	v_lshl_add_u64 v[216:217], s[38:39], 0, v[162:163]
	s_mov_b32 m0, s51
	s_nop 0
	global_load_lds_dwordx4 v[216:217], off
	s_waitcnt vmcnt(8)
	s_waitcnt lgkmcnt(0)
	s_barrier
	s_setprio 1
	s_waitcnt lgkmcnt(0)
	v_mfma_f32_16x16x128_f8f6f4 v[122:125], v[10:17], v[200:207], v[122:125]
	v_mfma_f32_16x16x128_f8f6f4 v[126:129], v[2:9], v[200:207], v[126:129]
	v_mfma_f32_16x16x128_f8f6f4 v[158:161], v[2:9], v[184:191], v[158:161]
	v_mfma_f32_16x16x128_f8f6f4 v[154:157], v[10:17], v[184:191], v[154:157]
	v_mfma_f32_16x16x128_f8f6f4 v[138:141], v[10:17], v[192:199], v[138:141]
	v_mfma_f32_16x16x128_f8f6f4 v[142:145], v[2:9], v[192:199], v[142:145]
	v_mfma_f32_16x16x128_f8f6f4 v[110:113], v[2:9], v[208:215], v[110:113]
	v_mfma_f32_16x16x128_f8f6f4 v[106:109], v[10:17], v[208:215], v[106:109]
	s_setprio 0
	s_setprio 1
	v_mfma_f32_16x16x128_f8f6f4 v[102:105], v[18:25], v[208:215], v[102:105]
	v_mfma_f32_16x16x128_f8f6f4 v[98:101], v[26:33], v[208:215], v[98:101]
	v_mfma_f32_16x16x128_f8f6f4 v[146:149], v[26:33], v[184:191], v[146:149]
	v_mfma_f32_16x16x128_f8f6f4 v[150:153], v[18:25], v[184:191], v[150:153]
	v_mfma_f32_16x16x128_f8f6f4 v[134:137], v[18:25], v[192:199], v[134:137]
	v_mfma_f32_16x16x128_f8f6f4 v[130:133], v[26:33], v[192:199], v[130:133]
	v_mfma_f32_16x16x128_f8f6f4 v[114:117], v[26:33], v[200:207], v[114:117]
	v_mfma_f32_16x16x128_f8f6f4 v[118:121], v[18:25], v[200:207], v[118:121]
	s_setprio 0
	s_barrier
	s_mov_b32 m0, s69
	v_lshl_add_u64 v[170:171], v[170:171], 0, s[8:9]
	ds_read_b128 v[184:187], v183 offset:49152
	ds_read_b128 v[188:191], v183 offset:50176
	ds_read_b128 v[192:195], v183 offset:51200
	ds_read_b128 v[196:199], v183 offset:52224
	ds_read_b128 v[200:203], v183 offset:53248
	ds_read_b128 v[204:207], v183 offset:54272
	ds_read_b128 v[208:211], v183 offset:55296
	ds_read_b128 v[212:215], v183 offset:56320
	global_load_lds_dwordx4 v[170:171], off
	v_lshl_add_u64 v[170:171], v[172:173], 0, s[8:9]
	s_mov_b32 m0, s67
	s_nop 0
	global_load_lds_dwordx4 v[170:171], off
	v_lshl_add_u64 v[170:171], s[36:37], 0, v[164:165]
	s_mov_b32 m0, s68
	s_nop 0
	global_load_lds_dwordx4 v[170:171], off
	v_lshl_add_u64 v[170:171], s[36:37], 0, v[162:163]
	s_mov_b32 m0, s66
	s_nop 0
	global_load_lds_dwordx4 v[170:171], off
	v_lshl_add_u64 v[170:171], v[174:175], 0, s[8:9]
	s_mov_b32 m0, s61
	s_nop 0
	global_load_lds_dwordx4 v[170:171], off
	v_lshl_add_u64 v[170:171], v[176:177], 0, s[8:9]
	s_mov_b32 m0, s62
	s_nop 0
	global_load_lds_dwordx4 v[170:171], off
	s_waitcnt vmcnt(8)
	s_waitcnt lgkmcnt(0)
	s_barrier
	s_setprio 1
	s_waitcnt lgkmcnt(0)
	v_mfma_f32_16x16x128_f8f6f4 v[62:65], v[2:9], v[200:207], v[62:65]
	v_mfma_f32_16x16x128_f8f6f4 v[58:61], v[10:17], v[200:207], v[58:61]
	v_mfma_f32_16x16x128_f8f6f4 v[90:93], v[10:17], v[184:191], v[90:93]
	v_mfma_f32_16x16x128_f8f6f4 v[94:97], v[2:9], v[184:191], v[94:97]
	v_mfma_f32_16x16x128_f8f6f4 v[78:81], v[2:9], v[192:199], v[78:81]
	v_mfma_f32_16x16x128_f8f6f4 v[74:77], v[10:17], v[192:199], v[74:77]
	v_mfma_f32_16x16x128_f8f6f4 v[42:45], v[10:17], v[208:215], v[42:45]
	v_mfma_f32_16x16x128_f8f6f4 v[54:57], v[2:9], v[208:215], v[54:57]
	s_setprio 0
	s_setprio 1
	v_mfma_f32_16x16x128_f8f6f4 v[38:41], v[18:25], v[208:215], v[38:41]
	v_mfma_f32_16x16x128_f8f6f4 v[34:37], v[26:33], v[208:215], v[34:37]
	v_mfma_f32_16x16x128_f8f6f4 v[82:85], v[26:33], v[184:191], v[82:85]
	v_mfma_f32_16x16x128_f8f6f4 v[86:89], v[18:25], v[184:191], v[86:89]
	v_mfma_f32_16x16x128_f8f6f4 v[70:73], v[18:25], v[192:199], v[70:73]
	v_mfma_f32_16x16x128_f8f6f4 v[66:69], v[26:33], v[192:199], v[66:69]
	v_mfma_f32_16x16x128_f8f6f4 v[46:49], v[26:33], v[200:207], v[46:49]
	v_mfma_f32_16x16x128_f8f6f4 v[50:53], v[18:25], v[200:207], v[50:53]
	s_setprio 0
	s_barrier
	s_movk_i32 s38, 0x100
	s_andn2_b64 vcc, exec, s[34:35]
	s_mov_b64 s[36:37], -1
	s_mov_b64 s[34:35], 0
	s_cbranch_vccz .LBB0_1558
	s_and_b64 vcc, exec, s[12:13]
	s_cbranch_vccz .LBB0_1561
	s_barrier

.LBB0_1681:
	ds_read_b128 v[26:29], v189
	ds_read_b128 v[30:33], v189 offset:1024
	ds_read_b128 v[18:21], v189 offset:2048
	ds_read_b128 v[22:25], v189 offset:3072
	ds_read_b128 v[10:13], v190
	ds_read_b128 v[14:17], v190 offset:1024
	ds_read_b128 v[2:5], v190 offset:2048
	ds_read_b128 v[6:9], v190 offset:3072
	s_add_u32 s34, s30, 0xfff80080
	s_addc_u32 s35, s31, -1
	s_cmp_eq_u32 s60, 28
	s_cselect_b32 s37, s18, s35
	s_cselect_b32 s36, s19, s34
	s_cselect_b32 s35, s21, s59
	s_cselect_b32 s34, s23, s58
	s_mov_b32 m0, s43
	s_nop 0
	global_load_lds_dwordx4 v168, s[100:101]
	s_mov_b32 m0, s44
	s_nop 0
	global_load_lds_dwordx4 v164, s[100:101]
	s_add_i32 m0, s29, 0xc000
	ds_read_b128 v[178:181], v191
	ds_read_b128 v[182:185], v191 offset:1024
	ds_read_b128 v[194:197], v191 offset:2048
	ds_read_b128 v[198:201], v191 offset:3072
	ds_read_b128 v[202:205], v191 offset:4096
	ds_read_b128 v[206:209], v191 offset:5120
	ds_read_b128 v[210:213], v191 offset:6144
	ds_read_b128 v[214:217], v191 offset:7168
	global_load_lds_dwordx4 v170, s[30:31]
	s_add_i32 m0, s29, 0xe000
	s_nop 0
	global_load_lds_dwordx4 v172, s[30:31]
	s_waitcnt vmcnt(8)
	s_waitcnt lgkmcnt(0)
	s_barrier
	s_setprio 1
	s_waitcnt lgkmcnt(0)
	v_mfma_f32_16x16x128_f8f6f4 v[158:161], v[26:33], v[178:185], v[158:161]
	v_mfma_f32_16x16x128_f8f6f4 v[154:157], v[18:25], v[178:185], v[154:157]
	v_mfma_f32_16x16x128_f8f6f4 v[138:141], v[18:25], v[194:201], v[138:141]
	v_mfma_f32_16x16x128_f8f6f4 v[142:145], v[26:33], v[194:201], v[142:145]
	v_mfma_f32_16x16x128_f8f6f4 v[126:129], v[26:33], v[202:209], v[126:129]
	v_mfma_f32_16x16x128_f8f6f4 v[122:125], v[18:25], v[202:209], v[122:125]
	v_mfma_f32_16x16x128_f8f6f4 v[106:109], v[18:25], v[210:217], v[106:109]
	v_mfma_f32_16x16x128_f8f6f4 v[110:113], v[26:33], v[210:217], v[110:113]
	s_setprio 0
	s_setprio 1
	v_mfma_f32_16x16x128_f8f6f4 v[102:105], v[10:17], v[210:217], v[102:105]
	v_mfma_f32_16x16x128_f8f6f4 v[98:101], v[2:9], v[210:217], v[98:101]
	v_mfma_f32_16x16x128_f8f6f4 v[146:149], v[2:9], v[178:185], v[146:149]
	v_mfma_f32_16x16x128_f8f6f4 v[150:153], v[10:17], v[178:185], v[150:153]
	v_mfma_f32_16x16x128_f8f6f4 v[134:137], v[10:17], v[194:201], v[134:137]
	v_mfma_f32_16x16x128_f8f6f4 v[130:133], v[2:9], v[194:201], v[130:133]
	v_mfma_f32_16x16x128_f8f6f4 v[114:117], v[2:9], v[202:209], v[114:117]
	v_mfma_f32_16x16x128_f8f6f4 v[118:121], v[10:17], v[202:209], v[118:121]
	s_setprio 0
	s_barrier
	s_add_i32 s61, s45, s3
	s_mov_b32 m0, s61
	ds_read_b128 v[194:197], v191 offset:16384
	ds_read_b128 v[198:201], v191 offset:17408
	ds_read_b128 v[202:205], v191 offset:18432
	ds_read_b128 v[206:209], v191 offset:19456
	ds_read_b128 v[210:213], v191 offset:20480
	ds_read_b128 v[214:217], v191 offset:21504
	ds_read_b128 v[218:221], v191 offset:22528
	ds_read_b128 v[222:225], v191 offset:23552
	global_load_lds_dwordx4 v166, s[34:35]
	s_add_i32 m0, s61, 0x2000
	s_add_u32 s62, s34, 0x80000
	s_addc_u32 s63, s35, 0
	s_add_i32 s61, s48, s3
	global_load_lds_dwordx4 v162, s[34:35]
	s_mov_b32 m0, s61
	s_nop 0
	global_load_lds_dwordx4 v166, s[62:63]
	s_add_i32 m0, s61, 0x2000
	s_nop 0
	global_load_lds_dwordx4 v162, s[62:63]
	s_waitcnt vmcnt(6)
	s_waitcnt lgkmcnt(0)
	s_barrier
	s_setprio 1
	s_waitcnt lgkmcnt(0)
	v_mfma_f32_16x16x128_f8f6f4 v[78:81], v[26:33], v[202:209], v[78:81]
	v_mfma_f32_16x16x128_f8f6f4 v[74:77], v[18:25], v[202:209], v[74:77]
	v_mfma_f32_16x16x128_f8f6f4 v[90:93], v[18:25], v[194:201], v[90:93]
	v_mfma_f32_16x16x128_f8f6f4 v[94:97], v[26:33], v[194:201], v[94:97]
	v_mfma_f32_16x16x128_f8f6f4 v[62:65], v[26:33], v[210:217], v[62:65]
	v_mfma_f32_16x16x128_f8f6f4 v[58:61], v[18:25], v[210:217], v[58:61]
	v_mfma_f32_16x16x128_f8f6f4 v[42:45], v[18:25], v[218:225], v[42:45]
	v_mfma_f32_16x16x128_f8f6f4 v[46:49], v[26:33], v[218:225], v[46:49]
	s_setprio 0
	s_setprio 1
	v_mfma_f32_16x16x128_f8f6f4 v[38:41], v[10:17], v[218:225], v[38:41]
	v_mfma_f32_16x16x128_f8f6f4 v[34:37], v[2:9], v[218:225], v[34:37]
	v_mfma_f32_16x16x128_f8f6f4 v[82:85], v[2:9], v[194:201], v[82:85]
	v_mfma_f32_16x16x128_f8f6f4 v[86:89], v[10:17], v[194:201], v[86:89]
	v_mfma_f32_16x16x128_f8f6f4 v[70:73], v[10:17], v[202:209], v[70:73]
	v_mfma_f32_16x16x128_f8f6f4 v[66:69], v[2:9], v[202:209], v[66:69]
	v_mfma_f32_16x16x128_f8f6f4 v[50:53], v[2:9], v[210:217], v[50:53]
	v_mfma_f32_16x16x128_f8f6f4 v[54:57], v[10:17], v[210:217], v[54:57]
	s_setprio 0
	s_barrier
	s_add_i32 s61, 0, 0x18000
	s_add_i32 s62, 0, 0x1c000
	v_add_u32_e32 v14, s61, v187
	v_add_u32_e32 v30, s62, v187
	ds_read_b128 v[2:5], v14
	ds_read_b128 v[6:9], v14 offset:1024
	ds_read_b128 v[10:13], v14 offset:2048
	ds_read_b128 v[14:17], v14 offset:3072
	ds_read_b128 v[18:21], v30
	ds_read_b128 v[22:25], v30 offset:1024
	ds_read_b128 v[26:29], v30 offset:2048
	ds_read_b128 v[30:33], v30 offset:3072
	s_mov_b32 m0, s29
	s_nop 0
	global_load_lds_dwordx4 v168, s[36:37]
	s_mov_b32 m0, s38
	s_nop 0
	global_load_lds_dwordx4 v164, s[36:37]
	s_add_u32 s36, s36, 0x80000
	s_addc_u32 s37, s37, 0
	s_add_u32 s100, s36, 0xfff80080
	s_addc_u32 s101, s37, -1
	s_mov_b32 m0, s39
	ds_read_b128 v[194:197], v191 offset:32768
	ds_read_b128 v[198:201], v191 offset:33792
	ds_read_b128 v[202:205], v191 offset:34816
	ds_read_b128 v[206:209], v191 offset:35840
	ds_read_b128 v[210:213], v191 offset:36864
	ds_read_b128 v[214:217], v191 offset:37888
	ds_read_b128 v[218:221], v191 offset:38912
	ds_read_b128 v[222:225], v191 offset:39936
	global_load_lds_dwordx4 v168, s[36:37]
	s_mov_b32 m0, s40
	s_nop 0
	global_load_lds_dwordx4 v164, s[36:37]
	s_waitcnt vmcnt(8)
	s_waitcnt lgkmcnt(0)
	s_barrier
	s_setprio 1
	s_waitcnt lgkmcnt(0)
	v_mfma_f32_16x16x128_f8f6f4 v[122:125], v[10:17], v[210:217], v[122:125]
	v_mfma_f32_16x16x128_f8f6f4 v[126:129], v[2:9], v[210:217], v[126:129]
	v_mfma_f32_16x16x128_f8f6f4 v[158:161], v[2:9], v[194:201], v[158:161]
	v_mfma_f32_16x16x128_f8f6f4 v[154:157], v[10:17], v[194:201], v[154:157]
	v_mfma_f32_16x16x128_f8f6f4 v[138:141], v[10:17], v[202:209], v[138:141]
	v_mfma_f32_16x16x128_f8f6f4 v[142:145], v[2:9], v[202:209], v[142:145]
	v_mfma_f32_16x16x128_f8f6f4 v[110:113], v[2:9], v[218:225], v[110:113]
	v_mfma_f32_16x16x128_f8f6f4 v[106:109], v[10:17], v[218:225], v[106:109]
	s_setprio 0
	s_setprio 1
	v_mfma_f32_16x16x128_f8f6f4 v[102:105], v[18:25], v[218:225], v[102:105]
	v_mfma_f32_16x16x128_f8f6f4 v[98:101], v[26:33], v[218:225], v[98:101]
	v_mfma_f32_16x16x128_f8f6f4 v[146:149], v[26:33], v[194:201], v[146:149]
	v_mfma_f32_16x16x128_f8f6f4 v[150:153], v[18:25], v[194:201], v[150:153]
	v_mfma_f32_16x16x128_f8f6f4 v[134:137], v[18:25], v[202:209], v[134:137]
	v_mfma_f32_16x16x128_f8f6f4 v[130:133], v[26:33], v[202:209], v[130:133]
	v_mfma_f32_16x16x128_f8f6f4 v[114:117], v[26:33], v[210:217], v[114:117]
	v_mfma_f32_16x16x128_f8f6f4 v[118:121], v[18:25], v[210:217], v[118:121]
	s_setprio 0
	s_barrier
	s_add_i32 s36, s61, s3
	s_mov_b32 m0, s36
	s_add_u32 s98, s34, 0x80
	s_addc_u32 s99, s35, 0
	ds_read_b128 v[194:197], v191 offset:49152
	ds_read_b128 v[198:201], v191 offset:50176
	ds_read_b128 v[202:205], v191 offset:51200
	ds_read_b128 v[206:209], v191 offset:52224
	ds_read_b128 v[210:213], v191 offset:53248
	ds_read_b128 v[214:217], v191 offset:54272
	ds_read_b128 v[218:221], v191 offset:55296
	ds_read_b128 v[222:225], v191 offset:56320
	global_load_lds_dwordx4 v166, s[98:99]
	s_add_i32 m0, s36, 0x2000
	s_add_u32 s34, s34, 0x80080
	s_addc_u32 s35, s35, 0
	s_add_i32 s36, s62, s3
	global_load_lds_dwordx4 v162, s[98:99]
	s_mov_b32 m0, s36
	s_nop 0
	global_load_lds_dwordx4 v166, s[34:35]
	s_add_i32 m0, s36, 0x2000
	s_nop 0
	global_load_lds_dwordx4 v162, s[34:35]
	s_waitcnt vmcnt(6)
	s_waitcnt lgkmcnt(0)
	s_barrier
	s_setprio 1
	s_waitcnt lgkmcnt(0)
	v_mfma_f32_16x16x128_f8f6f4 v[62:65], v[2:9], v[210:217], v[62:65]
	v_mfma_f32_16x16x128_f8f6f4 v[58:61], v[10:17], v[210:217], v[58:61]
	v_mfma_f32_16x16x128_f8f6f4 v[90:93], v[10:17], v[194:201], v[90:93]
	v_mfma_f32_16x16x128_f8f6f4 v[94:97], v[2:9], v[194:201], v[94:97]
	v_mfma_f32_16x16x128_f8f6f4 v[78:81], v[2:9], v[202:209], v[78:81]
	v_mfma_f32_16x16x128_f8f6f4 v[74:77], v[10:17], v[202:209], v[74:77]
	v_mfma_f32_16x16x128_f8f6f4 v[42:45], v[10:17], v[218:225], v[42:45]
	v_mfma_f32_16x16x128_f8f6f4 v[46:49], v[2:9], v[218:225], v[46:49]
	s_setprio 0
	s_setprio 1
	v_mfma_f32_16x16x128_f8f6f4 v[38:41], v[18:25], v[218:225], v[38:41]
	v_mfma_f32_16x16x128_f8f6f4 v[34:37], v[26:33], v[218:225], v[34:37]
	v_mfma_f32_16x16x128_f8f6f4 v[82:85], v[26:33], v[194:201], v[82:85]
	v_mfma_f32_16x16x128_f8f6f4 v[86:89], v[18:25], v[194:201], v[86:89]
	v_mfma_f32_16x16x128_f8f6f4 v[70:73], v[18:25], v[202:209], v[70:73]
	v_mfma_f32_16x16x128_f8f6f4 v[66:69], v[26:33], v[202:209], v[66:69]
	v_mfma_f32_16x16x128_f8f6f4 v[50:53], v[26:33], v[210:217], v[50:53]
	v_mfma_f32_16x16x128_f8f6f4 v[54:57], v[18:25], v[210:217], v[54:57]
	s_setprio 0
	s_barrier
	s_add_i32 s60, s60, 2
	s_add_u32 s30, s30, 0x100
	s_addc_u32 s31, s31, 0
	s_add_u32 s58, s58, 0x100
	s_addc_u32 s59, s59, 0
	s_cmp_gt_u32 s60, 29
	s_cbranch_scc0 .LBB0_1681
	s_and_b64 vcc, exec, s[12:13]
	s_cbranch_vccz .LBB0_1684
	s_barrier

.LBB0_1807:
	ds_read_b128 v[26:29], v185
	ds_read_b128 v[30:33], v185 offset:1024
	ds_read_b128 v[18:21], v185 offset:2048
	ds_read_b128 v[22:25], v185 offset:3072
	ds_read_b128 v[10:13], v186
	ds_read_b128 v[14:17], v186 offset:1024
	ds_read_b128 v[2:5], v186 offset:2048
	ds_read_b128 v[6:9], v186 offset:3072
	s_add_u32 s28, s26, 0xffea8080
	s_addc_u32 s29, s27, -1
	s_cmpk_eq_i32 s58, 0x52
	s_cselect_b32 s31, s5, s29
	s_cselect_b32 s30, s4, s28
	s_cselect_b32 s29, s25, s57
	s_cselect_b32 s28, s24, s56
	v_lshl_add_u64 v[212:213], s[26:27], 0, v[166:167]
	s_add_i32 m0, s34, 0xc000
	ds_read_b128 v[174:177], v187
	ds_read_b128 v[178:181], v187 offset:1024
	ds_read_b128 v[188:191], v187 offset:2048
	ds_read_b128 v[192:195], v187 offset:3072
	ds_read_b128 v[196:199], v187 offset:4096
	ds_read_b128 v[200:203], v187 offset:5120
	ds_read_b128 v[204:207], v187 offset:6144
	ds_read_b128 v[208:211], v187 offset:7168
	global_load_lds_dwordx4 v[212:213], off
	v_lshl_add_u64 v[212:213], s[26:27], 0, v[168:169]
	s_add_i32 m0, s34, 0xe000
	s_nop 0
	global_load_lds_dwordx4 v[212:213], off
	s_waitcnt vmcnt(8)
	s_waitcnt lgkmcnt(0)
	s_barrier
	s_setprio 1
	s_waitcnt lgkmcnt(0)
	v_mfma_f32_16x16x128_f8f6f4 v[158:161], v[26:33], v[174:181], v[158:161]
	v_mfma_f32_16x16x128_f8f6f4 v[154:157], v[18:25], v[174:181], v[154:157]
	v_mfma_f32_16x16x128_f8f6f4 v[138:141], v[18:25], v[188:195], v[138:141]
	v_mfma_f32_16x16x128_f8f6f4 v[142:145], v[26:33], v[188:195], v[142:145]
	v_mfma_f32_16x16x128_f8f6f4 v[126:129], v[26:33], v[196:203], v[126:129]
	v_mfma_f32_16x16x128_f8f6f4 v[122:125], v[18:25], v[196:203], v[122:125]
	v_mfma_f32_16x16x128_f8f6f4 v[106:109], v[18:25], v[204:211], v[106:109]
	v_mfma_f32_16x16x128_f8f6f4 v[110:113], v[26:33], v[204:211], v[110:113]
	s_setprio 0
	s_setprio 1
	v_mfma_f32_16x16x128_f8f6f4 v[102:105], v[10:17], v[204:211], v[102:105]
	v_mfma_f32_16x16x128_f8f6f4 v[98:101], v[2:9], v[204:211], v[98:101]
	v_mfma_f32_16x16x128_f8f6f4 v[146:149], v[2:9], v[174:181], v[146:149]
	v_mfma_f32_16x16x128_f8f6f4 v[150:153], v[10:17], v[174:181], v[150:153]
	v_mfma_f32_16x16x128_f8f6f4 v[134:137], v[10:17], v[188:195], v[134:137]
	v_mfma_f32_16x16x128_f8f6f4 v[130:133], v[2:9], v[188:195], v[130:133]
	v_mfma_f32_16x16x128_f8f6f4 v[114:117], v[2:9], v[196:203], v[114:117]
	v_mfma_f32_16x16x128_f8f6f4 v[118:121], v[10:17], v[196:203], v[118:121]
	s_setprio 0
	s_barrier
	s_add_i32 s59, s42, s3
	v_lshl_add_u64 v[174:175], s[28:29], 0, v[164:165]
	s_mov_b32 m0, s59
	ds_read_b128 v[188:191], v187 offset:16384
	ds_read_b128 v[192:195], v187 offset:17408
	ds_read_b128 v[196:199], v187 offset:18432
	ds_read_b128 v[200:203], v187 offset:19456
	ds_read_b128 v[204:207], v187 offset:20480
	ds_read_b128 v[208:211], v187 offset:21504
	ds_read_b128 v[212:215], v187 offset:22528
	ds_read_b128 v[216:219], v187 offset:23552
	global_load_lds_dwordx4 v[174:175], off
	s_add_i32 m0, s59, 0x2000
	s_add_u32 s60, s28, 0x158000
	v_lshl_add_u64 v[176:177], s[28:29], 0, v[162:163]
	s_addc_u32 s61, s29, 0
	s_add_i32 s59, s43, s3
	global_load_lds_dwordx4 v[176:177], off
	v_lshl_add_u64 v[178:179], s[60:61], 0, v[164:165]
	s_mov_b32 m0, s59
	v_lshl_add_u64 v[180:181], s[30:31], 0, v[162:163]
	global_load_lds_dwordx4 v[178:179], off
	v_lshl_add_u64 v[178:179], s[60:61], 0, v[162:163]
	s_add_i32 m0, s59, 0x2000
	s_nop 0
	global_load_lds_dwordx4 v[178:179], off
	v_lshl_add_u64 v[178:179], s[30:31], 0, v[164:165]
	s_mov_b32 m0, s34
	s_nop 0
	global_load_lds_dwordx4 v[178:179], off
	s_mov_b32 m0, s35
	s_nop 0
	global_load_lds_dwordx4 v[180:181], off
	s_waitcnt vmcnt(8)
	s_waitcnt lgkmcnt(0)
	s_barrier
	s_setprio 1
	s_waitcnt lgkmcnt(0)
	v_mfma_f32_16x16x128_f8f6f4 v[78:81], v[26:33], v[196:203], v[78:81]
	v_mfma_f32_16x16x128_f8f6f4 v[74:77], v[18:25], v[196:203], v[74:77]
	v_mfma_f32_16x16x128_f8f6f4 v[90:93], v[18:25], v[188:195], v[90:93]
	v_mfma_f32_16x16x128_f8f6f4 v[94:97], v[26:33], v[188:195], v[94:97]
	v_mfma_f32_16x16x128_f8f6f4 v[62:65], v[26:33], v[204:211], v[62:65]
	v_mfma_f32_16x16x128_f8f6f4 v[58:61], v[18:25], v[204:211], v[58:61]
	v_mfma_f32_16x16x128_f8f6f4 v[42:45], v[18:25], v[212:219], v[42:45]
	v_mfma_f32_16x16x128_f8f6f4 v[54:57], v[26:33], v[212:219], v[54:57]
	s_setprio 0
	s_setprio 1
	v_mfma_f32_16x16x128_f8f6f4 v[38:41], v[10:17], v[212:219], v[38:41]
	v_mfma_f32_16x16x128_f8f6f4 v[34:37], v[2:9], v[212:219], v[34:37]
	v_mfma_f32_16x16x128_f8f6f4 v[82:85], v[2:9], v[188:195], v[82:85]
	v_mfma_f32_16x16x128_f8f6f4 v[86:89], v[10:17], v[188:195], v[86:89]
	v_mfma_f32_16x16x128_f8f6f4 v[70:73], v[10:17], v[196:203], v[70:73]
	v_mfma_f32_16x16x128_f8f6f4 v[66:69], v[2:9], v[196:203], v[66:69]
	v_mfma_f32_16x16x128_f8f6f4 v[46:49], v[2:9], v[204:211], v[46:49]
	v_mfma_f32_16x16x128_f8f6f4 v[50:53], v[10:17], v[204:211], v[50:53]
	s_setprio 0
	s_barrier
	s_add_i32 s59, 0, 0x18000
	s_add_i32 s60, 0, 0x1c000
	v_add_u32_e32 v14, s59, v183
	v_add_u32_e32 v30, s60, v183
	ds_read_b128 v[2:5], v14
	ds_read_b128 v[6:9], v14 offset:1024
	ds_read_b128 v[10:13], v14 offset:2048
	ds_read_b128 v[14:17], v14 offset:3072
	ds_read_b128 v[18:21], v30
	ds_read_b128 v[22:25], v30 offset:1024
	ds_read_b128 v[26:29], v30 offset:2048
	ds_read_b128 v[30:33], v30 offset:3072
	s_add_u32 s30, s30, 0x158000
	s_addc_u32 s31, s31, 0
	s_mov_b32 m0, s36
	v_lshl_add_u64 v[220:221], s[30:31], 0, v[164:165]
	ds_read_b128 v[188:191], v187 offset:32768
	ds_read_b128 v[192:195], v187 offset:33792
	ds_read_b128 v[196:199], v187 offset:34816
	ds_read_b128 v[200:203], v187 offset:35840
	ds_read_b128 v[204:207], v187 offset:36864
	ds_read_b128 v[208:211], v187 offset:37888
	ds_read_b128 v[212:215], v187 offset:38912
	ds_read_b128 v[216:219], v187 offset:39936
	global_load_lds_dwordx4 v[220:221], off
	v_lshl_add_u64 v[220:221], s[30:31], 0, v[162:163]
	s_mov_b32 m0, s37
	s_nop 0
	global_load_lds_dwordx4 v[220:221], off
	s_waitcnt vmcnt(8)
	s_waitcnt lgkmcnt(0)
	s_barrier
	s_setprio 1
	s_waitcnt lgkmcnt(0)
	v_mfma_f32_16x16x128_f8f6f4 v[122:125], v[10:17], v[204:211], v[122:125]
	v_mfma_f32_16x16x128_f8f6f4 v[126:129], v[2:9], v[204:211], v[126:129]
	v_mfma_f32_16x16x128_f8f6f4 v[158:161], v[2:9], v[188:195], v[158:161]
	v_mfma_f32_16x16x128_f8f6f4 v[154:157], v[10:17], v[188:195], v[154:157]
	v_mfma_f32_16x16x128_f8f6f4 v[138:141], v[10:17], v[196:203], v[138:141]
	v_mfma_f32_16x16x128_f8f6f4 v[142:145], v[2:9], v[196:203], v[142:145]
	v_mfma_f32_16x16x128_f8f6f4 v[110:113], v[2:9], v[212:219], v[110:113]
	v_mfma_f32_16x16x128_f8f6f4 v[106:109], v[10:17], v[212:219], v[106:109]
	s_setprio 0
	s_setprio 1
	v_mfma_f32_16x16x128_f8f6f4 v[102:105], v[18:25], v[212:219], v[102:105]
	v_mfma_f32_16x16x128_f8f6f4 v[98:101], v[26:33], v[212:219], v[98:101]
	v_mfma_f32_16x16x128_f8f6f4 v[146:149], v[26:33], v[188:195], v[146:149]
	v_mfma_f32_16x16x128_f8f6f4 v[150:153], v[18:25], v[188:195], v[150:153]
	v_mfma_f32_16x16x128_f8f6f4 v[134:137], v[18:25], v[196:203], v[134:137]
	v_mfma_f32_16x16x128_f8f6f4 v[130:133], v[26:33], v[196:203], v[130:133]
	v_mfma_f32_16x16x128_f8f6f4 v[114:117], v[26:33], v[204:211], v[114:117]
	v_mfma_f32_16x16x128_f8f6f4 v[118:121], v[18:25], v[204:211], v[118:121]
	s_setprio 0
	s_barrier
	s_add_i32 s30, s59, s3
	v_lshl_add_u64 v[174:175], v[174:175], 0, s[10:11]
	s_mov_b32 m0, s30
	ds_read_b128 v[188:191], v187 offset:49152
	ds_read_b128 v[192:195], v187 offset:50176
	ds_read_b128 v[196:199], v187 offset:51200
	ds_read_b128 v[200:203], v187 offset:52224
	ds_read_b128 v[204:207], v187 offset:53248
	ds_read_b128 v[208:211], v187 offset:54272
	ds_read_b128 v[212:215], v187 offset:55296
	ds_read_b128 v[216:219], v187 offset:56320
	global_load_lds_dwordx4 v[174:175], off
	s_add_i32 m0, s30, 0x2000
	s_add_u32 s28, s28, 0x158080
	v_lshl_add_u64 v[174:175], v[176:177], 0, s[10:11]
	s_addc_u32 s29, s29, 0
	s_add_i32 s30, s60, s3
	global_load_lds_dwordx4 v[174:175], off
	v_lshl_add_u64 v[174:175], s[28:29], 0, v[164:165]
	s_mov_b32 m0, s30
	s_nop 0
	global_load_lds_dwordx4 v[174:175], off
	v_lshl_add_u64 v[174:175], s[28:29], 0, v[162:163]
	s_add_i32 m0, s30, 0x2000
	s_nop 0
	global_load_lds_dwordx4 v[174:175], off
	v_lshl_add_u64 v[174:175], v[178:179], 0, s[10:11]
	s_mov_b32 m0, s40
	s_nop 0
	global_load_lds_dwordx4 v[174:175], off
	v_lshl_add_u64 v[174:175], v[180:181], 0, s[10:11]
	s_mov_b32 m0, s41
	s_nop 0
	global_load_lds_dwordx4 v[174:175], off
	s_waitcnt vmcnt(8)
	s_waitcnt lgkmcnt(0)
	s_barrier
	s_setprio 1
	s_waitcnt lgkmcnt(0)
	v_mfma_f32_16x16x128_f8f6f4 v[62:65], v[2:9], v[204:211], v[62:65]
	v_mfma_f32_16x16x128_f8f6f4 v[58:61], v[10:17], v[204:211], v[58:61]
	v_mfma_f32_16x16x128_f8f6f4 v[90:93], v[10:17], v[188:195], v[90:93]
	v_mfma_f32_16x16x128_f8f6f4 v[94:97], v[2:9], v[188:195], v[94:97]
	v_mfma_f32_16x16x128_f8f6f4 v[78:81], v[2:9], v[196:203], v[78:81]
	v_mfma_f32_16x16x128_f8f6f4 v[74:77], v[10:17], v[196:203], v[74:77]
	v_mfma_f32_16x16x128_f8f6f4 v[42:45], v[10:17], v[212:219], v[42:45]
	v_mfma_f32_16x16x128_f8f6f4 v[54:57], v[2:9], v[212:219], v[54:57]
	s_setprio 0
	s_setprio 1
	v_mfma_f32_16x16x128_f8f6f4 v[38:41], v[18:25], v[212:219], v[38:41]
	v_mfma_f32_16x16x128_f8f6f4 v[34:37], v[26:33], v[212:219], v[34:37]
	v_mfma_f32_16x16x128_f8f6f4 v[82:85], v[26:33], v[188:195], v[82:85]
	v_mfma_f32_16x16x128_f8f6f4 v[86:89], v[18:25], v[188:195], v[86:89]
	v_mfma_f32_16x16x128_f8f6f4 v[70:73], v[18:25], v[196:203], v[70:73]
	v_mfma_f32_16x16x128_f8f6f4 v[66:69], v[26:33], v[196:203], v[66:69]
	v_mfma_f32_16x16x128_f8f6f4 v[46:49], v[26:33], v[204:211], v[46:49]
	v_mfma_f32_16x16x128_f8f6f4 v[50:53], v[18:25], v[204:211], v[50:53]
	s_setprio 0
	s_barrier
	s_add_i32 s58, s58, 2
	s_add_u32 s26, s26, 0x100
	s_addc_u32 s27, s27, 0
	s_add_u32 s56, s56, 0x100
	s_addc_u32 s57, s57, 0
	s_cmpk_gt_u32 s58, 0x53
	s_cbranch_scc0 .LBB0_1807
	s_and_b64 vcc, exec, s[12:13]
	s_cbranch_vccz .LBB0_1810
	s_barrier
